# GEMM main loops: per-half-tile LDS-DMA retirement (vmcnt(10) before the closing barrier of phases 1,2,4,5,6,8) instead of whole-buffer vmcnt(6) at phases 4 and 8
# baseline (speedup 1.0000x reference)
.LBB0_371:
	s_add_i32 s31, s24, 2
	s_add_u32 s45, s56, s29
	s_addc_u32 s25, s57, s30
	s_add_i32 s64, 0, 0x10000
	v_add_u32_e32 v0, s64, v139
	s_add_u32 s66, s20, s29
	ds_read_b128 v[146:149], v0
	ds_read_b128 v[150:153], v0 offset:1024
	ds_read_b128 v[154:157], v0 offset:2048
	ds_read_b128 v[158:161], v0 offset:3072
	s_addc_u32 s67, s21, s30
	s_add_u32 s66, s66, 0xffffff80
	s_addc_u32 s67, s67, -1
	s_add_i32 s71, s64, s26
	s_add_i32 m0, s46, 0xc000
	s_add_i32 s70, s46, 0xe000
	s_add_i32 s81, 0, 0x14000
	s_add_i32 s84, s71, 0x2000
	s_cmp_eq_u32 s79, s24
	s_cselect_b32 s24, s42, s45
	s_cselect_b32 s25, s43, s25
	s_cselect_b32 s45, 0, s30
	s_cselect_b32 s64, 0, s29
	v_mov_b32_e32 v0, v134
	ds_read_b128 v[162:165], v141
	ds_read_b128 v[166:169], v141 offset:1024
	ds_read_b128 v[170:173], v141 offset:2048
	ds_read_b128 v[190:193], v141 offset:3072
	ds_read_b128 v[194:197], v141 offset:4096
	ds_read_b128 v[198:201], v141 offset:5120
	ds_read_b128 v[202:205], v141 offset:6144
	ds_read_b128 v[206:209], v141 offset:7168
	s_nop 0
	global_load_lds_dwordx4 v0, s[66:67]
	v_mov_b32_e32 v0, v136
	s_mov_b32 m0, s70
	s_nop 0
	global_load_lds_dwordx4 v0, s[66:67]
	s_waitcnt lgkmcnt(8)
	s_barrier
	s_waitcnt lgkmcnt(0)
	s_setprio 1
	s_waitcnt lgkmcnt(0)
	v_mfma_f32_16x16x32_bf16 v[120:123], v[146:149], v[162:165], v[120:123]
	v_mfma_f32_16x16x32_bf16 v[116:119], v[154:157], v[162:165], v[116:119]
	v_mfma_f32_16x16x32_bf16 v[104:107], v[146:149], v[170:173], v[104:107]
	v_mfma_f32_16x16x32_bf16 v[100:103], v[154:157], v[170:173], v[100:103]
	v_mfma_f32_16x16x32_bf16 v[92:95], v[146:149], v[194:197], v[92:95]
	v_mfma_f32_16x16x32_bf16 v[84:87], v[154:157], v[194:197], v[84:87]
	v_mfma_f32_16x16x32_bf16 v[76:79], v[146:149], v[202:205], v[76:79]
	v_mfma_f32_16x16x32_bf16 v[68:71], v[154:157], v[202:205], v[68:71]
	v_mfma_f32_16x16x32_bf16 v[120:123], v[150:153], v[166:169], v[120:123]
	v_mfma_f32_16x16x32_bf16 v[116:119], v[158:161], v[166:169], v[116:119]
	v_mfma_f32_16x16x32_bf16 v[104:107], v[150:153], v[190:193], v[104:107]
	v_mfma_f32_16x16x32_bf16 v[100:103], v[158:161], v[190:193], v[100:103]
	v_mfma_f32_16x16x32_bf16 v[92:95], v[150:153], v[198:201], v[92:95]
	v_mfma_f32_16x16x32_bf16 v[84:87], v[158:161], v[198:201], v[84:87]
	v_mfma_f32_16x16x32_bf16 v[76:79], v[150:153], v[206:209], v[76:79]
	v_mfma_f32_16x16x32_bf16 v[68:71], v[158:161], v[206:209], v[68:71]
	s_setprio 0
	s_waitcnt vmcnt(10)
	s_barrier
	v_add_u32_e32 v0, s81, v139
	ds_read_b128 v[210:213], v0
	ds_read_b128 v[214:217], v0 offset:1024
	ds_read_b128 v[218:221], v0 offset:2048
	ds_read_b128 v[222:225], v0 offset:3072
	s_mov_b64 s[66:67], s[24:25]
	v_mov_b32_e32 v0, v135
	s_mov_b32 m0, s71
	s_nop 0
	global_load_lds_dwordx4 v0, s[66:67]
	v_mov_b32_e32 v0, v137
	s_mov_b32 m0, s84
	s_nop 0
	global_load_lds_dwordx4 v0, s[66:67]
	s_barrier
	s_waitcnt lgkmcnt(0)
	s_setprio 1
	s_waitcnt lgkmcnt(0)
	v_mfma_f32_16x16x32_bf16 v[128:131], v[210:213], v[162:165], v[128:131]
	v_mfma_f32_16x16x32_bf16 v[124:127], v[218:221], v[162:165], v[124:127]
	v_mfma_f32_16x16x32_bf16 v[112:115], v[210:213], v[170:173], v[112:115]
	v_mfma_f32_16x16x32_bf16 v[108:111], v[218:221], v[170:173], v[108:111]
	v_mfma_f32_16x16x32_bf16 v[96:99], v[210:213], v[194:197], v[96:99]
	v_mfma_f32_16x16x32_bf16 v[88:91], v[218:221], v[194:197], v[88:91]
	v_mfma_f32_16x16x32_bf16 v[80:83], v[210:213], v[202:205], v[80:83]
	v_mfma_f32_16x16x32_bf16 v[72:75], v[218:221], v[202:205], v[72:75]
	v_mfma_f32_16x16x32_bf16 v[128:131], v[214:217], v[166:169], v[128:131]
	v_mfma_f32_16x16x32_bf16 v[124:127], v[222:225], v[166:169], v[124:127]
	v_mfma_f32_16x16x32_bf16 v[112:115], v[214:217], v[190:193], v[112:115]
	v_mfma_f32_16x16x32_bf16 v[108:111], v[222:225], v[190:193], v[108:111]
	v_mfma_f32_16x16x32_bf16 v[96:99], v[214:217], v[198:201], v[96:99]
	v_mfma_f32_16x16x32_bf16 v[88:91], v[222:225], v[198:201], v[88:91]
	v_mfma_f32_16x16x32_bf16 v[80:83], v[214:217], v[206:209], v[80:83]
	v_mfma_f32_16x16x32_bf16 v[72:75], v[222:225], v[206:209], v[72:75]
	s_setprio 0
	s_cselect_b32 s85, s48, s58
	s_cselect_b32 s84, s49, s59
	s_add_u32 s66, s85, s64
	s_addc_u32 s67, s84, s45
	s_mov_b64 s[70:71], s[66:67]
	v_mov_b32_e32 v0, v134
	s_mov_b32 m0, s46
	s_waitcnt vmcnt(10)
	s_barrier
	ds_read_b128 v[162:165], v141 offset:16384
	ds_read_b128 v[166:169], v141 offset:17408
	ds_read_b128 v[170:173], v141 offset:18432
	ds_read_b128 v[190:193], v141 offset:19456
	ds_read_b128 v[194:197], v141 offset:20480
	ds_read_b128 v[198:201], v141 offset:21504
	ds_read_b128 v[202:205], v141 offset:22528
	ds_read_b128 v[206:209], v141 offset:23552
	s_nop 0
	global_load_lds_dwordx4 v0, s[70:71]
	v_mov_b32_e32 v0, v136
	s_mov_b32 m0, s47
	s_nop 0
	global_load_lds_dwordx4 v0, s[70:71]
	s_barrier
	s_waitcnt lgkmcnt(0)
	s_setprio 1
	s_waitcnt lgkmcnt(0)
	v_mfma_f32_16x16x32_bf16 v[56:59], v[146:149], v[162:165], v[56:59]
	v_mfma_f32_16x16x32_bf16 v[52:55], v[154:157], v[162:165], v[52:55]
	v_mfma_f32_16x16x32_bf16 v[40:43], v[146:149], v[170:173], v[40:43]
	v_mfma_f32_16x16x32_bf16 v[36:39], v[154:157], v[170:173], v[36:39]
	v_mfma_f32_16x16x32_bf16 v[24:27], v[146:149], v[194:197], v[24:27]
	v_mfma_f32_16x16x32_bf16 v[20:23], v[154:157], v[194:197], v[20:23]
	v_mfma_f32_16x16x32_bf16 v[12:15], v[146:149], v[202:205], v[12:15]
	v_mfma_f32_16x16x32_bf16 v[8:11], v[154:157], v[202:205], v[8:11]
	v_mfma_f32_16x16x32_bf16 v[56:59], v[150:153], v[166:169], v[56:59]
	v_mfma_f32_16x16x32_bf16 v[52:55], v[158:161], v[166:169], v[52:55]
	v_mfma_f32_16x16x32_bf16 v[40:43], v[150:153], v[190:193], v[40:43]
	v_mfma_f32_16x16x32_bf16 v[36:39], v[158:161], v[190:193], v[36:39]
	v_mfma_f32_16x16x32_bf16 v[24:27], v[150:153], v[198:201], v[24:27]
	v_mfma_f32_16x16x32_bf16 v[20:23], v[158:161], v[198:201], v[20:23]
	v_mfma_f32_16x16x32_bf16 v[12:15], v[150:153], v[206:209], v[12:15]
	v_mfma_f32_16x16x32_bf16 v[8:11], v[158:161], v[206:209], v[8:11]
	s_setprio 0
	s_barrier
	s_add_u32 s70, s24, s6
	s_addc_u32 s71, s25, s7
	v_mov_b32_e32 v0, v135
	s_add_i32 s81, s81, s26
	s_mov_b32 m0, s81
	s_nop 0
	global_load_lds_dwordx4 v0, s[70:71]
	v_mov_b32_e32 v0, v137
	s_add_i32 m0, s81, 0x2000
	s_nop 0
	global_load_lds_dwordx4 v0, s[70:71]
	s_barrier
	s_setprio 1
	v_mfma_f32_16x16x32_bf16 v[64:67], v[210:213], v[162:165], v[64:67]
	v_mfma_f32_16x16x32_bf16 v[60:63], v[218:221], v[162:165], v[60:63]
	v_mfma_f32_16x16x32_bf16 v[48:51], v[210:213], v[170:173], v[48:51]
	v_mfma_f32_16x16x32_bf16 v[44:47], v[218:221], v[170:173], v[44:47]
	v_mfma_f32_16x16x32_bf16 v[32:35], v[210:213], v[194:197], v[32:35]
	v_mfma_f32_16x16x32_bf16 v[28:31], v[218:221], v[194:197], v[28:31]
	v_mfma_f32_16x16x32_bf16 v[16:19], v[210:213], v[202:205], v[16:19]
	v_mfma_f32_16x16x32_bf16 v[4:7], v[218:221], v[202:205], v[4:7]
	v_mfma_f32_16x16x32_bf16 v[64:67], v[214:217], v[166:169], v[64:67]
	v_mfma_f32_16x16x32_bf16 v[60:63], v[222:225], v[166:169], v[60:63]
	v_mfma_f32_16x16x32_bf16 v[48:51], v[214:217], v[190:193], v[48:51]
	v_mfma_f32_16x16x32_bf16 v[44:47], v[222:225], v[190:193], v[44:47]
	v_mfma_f32_16x16x32_bf16 v[32:35], v[214:217], v[198:201], v[32:35]
	v_mfma_f32_16x16x32_bf16 v[28:31], v[222:225], v[198:201], v[28:31]
	v_mfma_f32_16x16x32_bf16 v[16:19], v[214:217], v[206:209], v[16:19]
	v_mfma_f32_16x16x32_bf16 v[4:7], v[222:225], v[206:209], v[4:7]
	s_setprio 0
	s_add_i32 s81, 0, 0x18000
	v_add_u32_e32 v0, s81, v139
	s_waitcnt vmcnt(10)
	s_barrier
	ds_read_b128 v[146:149], v0
	ds_read_b128 v[150:153], v0 offset:1024
	ds_read_b128 v[154:157], v0 offset:2048
	ds_read_b128 v[158:161], v0 offset:3072
	s_add_u32 s70, s85, s0
	s_addc_u32 s71, s84, s1
	s_add_u32 s70, s70, s64
	s_addc_u32 s71, s71, s45
	v_mov_b32_e32 v0, v134
	s_mov_b32 m0, s51
	ds_read_b128 v[162:165], v141 offset:32768
	ds_read_b128 v[166:169], v141 offset:33792
	ds_read_b128 v[170:173], v141 offset:34816
	ds_read_b128 v[190:193], v141 offset:35840
	ds_read_b128 v[194:197], v141 offset:36864
	ds_read_b128 v[198:201], v141 offset:37888
	ds_read_b128 v[202:205], v141 offset:38912
	ds_read_b128 v[206:209], v141 offset:39936
	s_nop 0
	global_load_lds_dwordx4 v0, s[70:71]
	v_mov_b32_e32 v0, v136
	s_mov_b32 m0, s53
	s_nop 0
	global_load_lds_dwordx4 v0, s[70:71]
	s_waitcnt lgkmcnt(8)
	s_barrier
	s_waitcnt lgkmcnt(0)
	s_setprio 1
	s_waitcnt lgkmcnt(0)
	v_mfma_f32_16x16x32_bf16 v[120:123], v[146:149], v[162:165], v[120:123]
	v_mfma_f32_16x16x32_bf16 v[116:119], v[154:157], v[162:165], v[116:119]
	v_mfma_f32_16x16x32_bf16 v[104:107], v[146:149], v[170:173], v[104:107]
	v_mfma_f32_16x16x32_bf16 v[100:103], v[154:157], v[170:173], v[100:103]
	v_mfma_f32_16x16x32_bf16 v[92:95], v[146:149], v[194:197], v[92:95]
	v_mfma_f32_16x16x32_bf16 v[84:87], v[154:157], v[194:197], v[84:87]
	v_mfma_f32_16x16x32_bf16 v[76:79], v[146:149], v[202:205], v[76:79]
	v_mfma_f32_16x16x32_bf16 v[68:71], v[154:157], v[202:205], v[68:71]
	v_mfma_f32_16x16x32_bf16 v[120:123], v[150:153], v[166:169], v[120:123]
	v_mfma_f32_16x16x32_bf16 v[116:119], v[158:161], v[166:169], v[116:119]
	v_mfma_f32_16x16x32_bf16 v[104:107], v[150:153], v[190:193], v[104:107]
	v_mfma_f32_16x16x32_bf16 v[100:103], v[158:161], v[190:193], v[100:103]
	v_mfma_f32_16x16x32_bf16 v[92:95], v[150:153], v[198:201], v[92:95]
	v_mfma_f32_16x16x32_bf16 v[84:87], v[158:161], v[198:201], v[84:87]
	v_mfma_f32_16x16x32_bf16 v[76:79], v[150:153], v[206:209], v[76:79]
	v_mfma_f32_16x16x32_bf16 v[68:71], v[158:161], v[206:209], v[68:71]
	s_setprio 0
	s_waitcnt vmcnt(10)
	s_barrier
	s_add_i32 s45, 0, 0x1c000
	s_add_u32 s24, s24, 0x80
	v_add_u32_e32 v0, s45, v139
	s_addc_u32 s25, s25, 0
	ds_read_b128 v[210:213], v0
	ds_read_b128 v[214:217], v0 offset:1024
	ds_read_b128 v[218:221], v0 offset:2048
	ds_read_b128 v[222:225], v0 offset:3072
	s_mov_b64 s[70:71], s[24:25]
	v_mov_b32_e32 v0, v135
	s_add_i32 s64, s81, s26
	s_mov_b32 m0, s64
	s_nop 0
	global_load_lds_dwordx4 v0, s[70:71]
	v_mov_b32_e32 v0, v137
	s_add_i32 m0, s64, 0x2000
	s_nop 0
	global_load_lds_dwordx4 v0, s[70:71]
	s_barrier
; template <class Epi, class Sched>
; __device__ __forceinline__ void gemm_phase(LAS unsigned char* lds, const int K_, const Sched& S, const Epi& E, const int wave_) {
;     ...
;         for (; t < nt; t += 2) { PG8_BODY(false); }
	s_waitcnt lgkmcnt(0)
	s_setprio 1
	s_waitcnt lgkmcnt(0)
	v_mfma_f32_16x16x32_bf16 v[128:131], v[210:213], v[162:165], v[128:131]
	v_mfma_f32_16x16x32_bf16 v[124:127], v[218:221], v[162:165], v[124:127]
	v_mfma_f32_16x16x32_bf16 v[112:115], v[210:213], v[170:173], v[112:115]
	v_mfma_f32_16x16x32_bf16 v[108:111], v[218:221], v[170:173], v[108:111]
	v_mfma_f32_16x16x32_bf16 v[96:99], v[210:213], v[194:197], v[96:99]
	v_mfma_f32_16x16x32_bf16 v[88:91], v[218:221], v[194:197], v[88:91]
	v_mfma_f32_16x16x32_bf16 v[80:83], v[210:213], v[202:205], v[80:83]
	v_mfma_f32_16x16x32_bf16 v[72:75], v[218:221], v[202:205], v[72:75]
	v_mfma_f32_16x16x32_bf16 v[128:131], v[214:217], v[166:169], v[128:131]
	v_mfma_f32_16x16x32_bf16 v[124:127], v[222:225], v[166:169], v[124:127]
	v_mfma_f32_16x16x32_bf16 v[112:115], v[214:217], v[190:193], v[112:115]
	v_mfma_f32_16x16x32_bf16 v[108:111], v[222:225], v[190:193], v[108:111]
	v_mfma_f32_16x16x32_bf16 v[96:99], v[214:217], v[198:201], v[96:99]
	v_mfma_f32_16x16x32_bf16 v[88:91], v[222:225], v[198:201], v[88:91]
	v_mfma_f32_16x16x32_bf16 v[80:83], v[214:217], v[206:209], v[80:83]
	v_mfma_f32_16x16x32_bf16 v[72:75], v[222:225], v[206:209], v[72:75]
	s_setprio 0
	s_add_u32 s66, s66, 0x80
	s_addc_u32 s67, s67, 0
	v_mov_b32_e32 v0, v134
	s_mov_b32 m0, s55
	s_waitcnt vmcnt(10)
	s_barrier
	ds_read_b128 v[162:165], v141 offset:49152
	ds_read_b128 v[166:169], v141 offset:50176
	ds_read_b128 v[170:173], v141 offset:51200
	ds_read_b128 v[190:193], v141 offset:52224
	ds_read_b128 v[194:197], v141 offset:53248
	ds_read_b128 v[198:201], v141 offset:54272
	ds_read_b128 v[202:205], v141 offset:55296
	ds_read_b128 v[206:209], v141 offset:56320
	s_nop 0
	global_load_lds_dwordx4 v0, s[66:67]
	v_mov_b32_e32 v0, v136
	s_mov_b32 m0, s69
	s_nop 0
	global_load_lds_dwordx4 v0, s[66:67]
	s_barrier
	s_waitcnt lgkmcnt(0)
	s_setprio 1
	s_waitcnt lgkmcnt(0)
	v_mfma_f32_16x16x32_bf16 v[56:59], v[146:149], v[162:165], v[56:59]
	v_mfma_f32_16x16x32_bf16 v[52:55], v[154:157], v[162:165], v[52:55]
	v_mfma_f32_16x16x32_bf16 v[40:43], v[146:149], v[170:173], v[40:43]
	v_mfma_f32_16x16x32_bf16 v[36:39], v[154:157], v[170:173], v[36:39]
	v_mfma_f32_16x16x32_bf16 v[24:27], v[146:149], v[194:197], v[24:27]
	v_mfma_f32_16x16x32_bf16 v[20:23], v[154:157], v[194:197], v[20:23]
	v_mfma_f32_16x16x32_bf16 v[12:15], v[146:149], v[202:205], v[12:15]
	v_mfma_f32_16x16x32_bf16 v[8:11], v[154:157], v[202:205], v[8:11]
	v_mfma_f32_16x16x32_bf16 v[56:59], v[150:153], v[166:169], v[56:59]
	v_mfma_f32_16x16x32_bf16 v[52:55], v[158:161], v[166:169], v[52:55]
	v_mfma_f32_16x16x32_bf16 v[40:43], v[150:153], v[190:193], v[40:43]
	v_mfma_f32_16x16x32_bf16 v[36:39], v[158:161], v[190:193], v[36:39]
	v_mfma_f32_16x16x32_bf16 v[24:27], v[150:153], v[198:201], v[24:27]
	v_mfma_f32_16x16x32_bf16 v[20:23], v[158:161], v[198:201], v[20:23]
	v_mfma_f32_16x16x32_bf16 v[12:15], v[150:153], v[206:209], v[12:15]
	v_mfma_f32_16x16x32_bf16 v[8:11], v[158:161], v[206:209], v[8:11]
	s_setprio 0
	s_barrier
	s_add_u32 s24, s24, s6
	s_addc_u32 s25, s25, s7
	v_mov_b32_e32 v0, v135
	s_add_i32 s45, s45, s26
	s_mov_b32 m0, s45
	s_nop 0
	global_load_lds_dwordx4 v0, s[24:25]
	v_mov_b32_e32 v0, v137
	s_add_i32 m0, s45, 0x2000
	s_nop 0
	global_load_lds_dwordx4 v0, s[24:25]
	s_barrier
	s_setprio 1
	v_mfma_f32_16x16x32_bf16 v[64:67], v[210:213], v[162:165], v[64:67]
	v_mfma_f32_16x16x32_bf16 v[60:63], v[218:221], v[162:165], v[60:63]
	v_mfma_f32_16x16x32_bf16 v[48:51], v[210:213], v[170:173], v[48:51]
	v_mfma_f32_16x16x32_bf16 v[44:47], v[218:221], v[170:173], v[44:47]
	v_mfma_f32_16x16x32_bf16 v[32:35], v[210:213], v[194:197], v[32:35]
	v_mfma_f32_16x16x32_bf16 v[28:31], v[218:221], v[194:197], v[28:31]
	v_mfma_f32_16x16x32_bf16 v[16:19], v[210:213], v[202:205], v[16:19]
	v_mfma_f32_16x16x32_bf16 v[4:7], v[218:221], v[202:205], v[4:7]
	v_mfma_f32_16x16x32_bf16 v[64:67], v[214:217], v[166:169], v[64:67]
	v_mfma_f32_16x16x32_bf16 v[60:63], v[222:225], v[166:169], v[60:63]
	v_mfma_f32_16x16x32_bf16 v[48:51], v[214:217], v[190:193], v[48:51]
	v_mfma_f32_16x16x32_bf16 v[44:47], v[222:225], v[190:193], v[44:47]
	v_mfma_f32_16x16x32_bf16 v[32:35], v[214:217], v[198:201], v[32:35]
	v_mfma_f32_16x16x32_bf16 v[28:31], v[222:225], v[198:201], v[28:31]
	v_mfma_f32_16x16x32_bf16 v[16:19], v[214:217], v[206:209], v[16:19]
	v_mfma_f32_16x16x32_bf16 v[4:7], v[222:225], v[206:209], v[4:7]
	s_setprio 0
	s_add_u32 s29, s29, 0x100
	s_addc_u32 s30, s30, 0
	s_cmp_lt_i32 s31, s54
	s_mov_b32 s24, s31
	s_waitcnt vmcnt(10)
	s_barrier
	s_cbranch_scc1 .LBB0_371
	s_waitcnt vmcnt(6)
	v_readlane_b32 s70, v254, 63
	v_readlane_b32 s71, v255, 0
	s_mul_i32 s81, s3, 24
	s_and_b64 vcc, exec, s[40:41]
	s_cbranch_vccz .LBB0_376
	s_branch .LBB0_377

.LBB0_1242:
	s_add_i32 s51, s64, 2
	s_add_u32 s66, s56, s24
	s_addc_u32 s67, s57, s25
	s_add_i32 s86, 0, 0x10000
	v_add_u32_e32 v0, s86, v163
	s_add_u32 s84, s21, s24
	ds_read_b128 v[132:135], v0
	ds_read_b128 v[136:139], v0 offset:1024
	ds_read_b128 v[140:143], v0 offset:2048
	ds_read_b128 v[146:149], v0 offset:3072
	s_addc_u32 s85, s49, s25
	s_add_u32 s84, s84, 0xffffff80
	s_addc_u32 s85, s85, -1
	s_add_i32 vcc_hi, s86, s17
	s_add_i32 m0, s30, 0xc000
	s_add_i32 s87, s30, 0xe000
	s_add_i32 vcc_lo, 0, 0x14000
	s_add_i32 s89, vcc_hi, 0x2000
	s_cmp_eq_u32 s79, s64
	s_cselect_b32 s64, 0, s25
	s_cselect_b32 s67, s43, s67
	s_cselect_b32 s66, s42, s66
	s_cselect_b32 s14, 0, s24
	v_mov_b32_e32 v0, v160
	ds_read_b128 v[150:153], v165
	ds_read_b128 v[154:157], v165 offset:1024
	ds_read_b128 v[166:169], v165 offset:2048
	ds_read_b128 v[170:173], v165 offset:3072
	ds_read_b128 v[190:193], v165 offset:4096
	ds_read_b128 v[194:197], v165 offset:5120
	ds_read_b128 v[198:201], v165 offset:6144
	ds_read_b128 v[202:205], v165 offset:7168
	s_nop 0
	global_load_lds_dwordx4 v0, s[84:85]
	v_mov_b32_e32 v0, v161
	s_mov_b32 m0, s87
	s_nop 0
	global_load_lds_dwordx4 v0, s[84:85]
	s_waitcnt lgkmcnt(8)
	s_barrier
	s_waitcnt lgkmcnt(0)
	s_setprio 1
	s_waitcnt lgkmcnt(0)
	v_mfma_f32_16x16x32_bf16 v[128:131], v[132:135], v[150:153], v[128:131]
	v_mfma_f32_16x16x32_bf16 v[96:99], v[140:143], v[150:153], v[96:99]
	v_mfma_f32_16x16x32_bf16 v[120:123], v[132:135], v[166:169], v[120:123]
	v_mfma_f32_16x16x32_bf16 v[88:91], v[140:143], v[166:169], v[88:91]
	v_mfma_f32_16x16x32_bf16 v[112:115], v[132:135], v[190:193], v[112:115]
	v_mfma_f32_16x16x32_bf16 v[80:83], v[140:143], v[190:193], v[80:83]
	v_mfma_f32_16x16x32_bf16 v[104:107], v[132:135], v[198:201], v[104:107]
	v_mfma_f32_16x16x32_bf16 v[72:75], v[140:143], v[198:201], v[72:75]
	v_mfma_f32_16x16x32_bf16 v[128:131], v[136:139], v[154:157], v[128:131]
	v_mfma_f32_16x16x32_bf16 v[96:99], v[146:149], v[154:157], v[96:99]
	v_mfma_f32_16x16x32_bf16 v[120:123], v[136:139], v[170:173], v[120:123]
	v_mfma_f32_16x16x32_bf16 v[88:91], v[146:149], v[170:173], v[88:91]
	v_mfma_f32_16x16x32_bf16 v[112:115], v[136:139], v[194:197], v[112:115]
	v_mfma_f32_16x16x32_bf16 v[80:83], v[146:149], v[194:197], v[80:83]
	v_mfma_f32_16x16x32_bf16 v[104:107], v[136:139], v[202:205], v[104:107]
	v_mfma_f32_16x16x32_bf16 v[72:75], v[146:149], v[202:205], v[72:75]
	s_setprio 0
	s_waitcnt vmcnt(10)
	s_barrier
	v_add_u32_e32 v0, vcc_lo, v163
	ds_read_b128 v[206:209], v0
	ds_read_b128 v[210:213], v0 offset:1024
	ds_read_b128 v[214:217], v0 offset:2048
	ds_read_b128 v[218:221], v0 offset:3072
	s_mov_b64 s[84:85], s[66:67]
	v_mov_b32_e32 v0, v160
	s_mov_b32 m0, vcc_hi
	s_nop 0
	global_load_lds_dwordx4 v0, s[84:85]
	v_mov_b32_e32 v0, v161
	s_mov_b32 m0, s89
	s_nop 0
	global_load_lds_dwordx4 v0, s[84:85]
	s_barrier
	s_waitcnt lgkmcnt(0)
	s_setprio 1
	s_waitcnt lgkmcnt(0)
	v_mfma_f32_16x16x32_bf16 v[64:67], v[206:209], v[150:153], v[64:67]
	v_mfma_f32_16x16x32_bf16 v[32:35], v[214:217], v[150:153], v[32:35]
	v_mfma_f32_16x16x32_bf16 v[56:59], v[206:209], v[166:169], v[56:59]
	v_mfma_f32_16x16x32_bf16 v[24:27], v[214:217], v[166:169], v[24:27]
	v_mfma_f32_16x16x32_bf16 v[48:51], v[206:209], v[190:193], v[48:51]
	v_mfma_f32_16x16x32_bf16 v[16:19], v[214:217], v[190:193], v[16:19]
	v_mfma_f32_16x16x32_bf16 v[40:43], v[206:209], v[198:201], v[40:43]
	v_mfma_f32_16x16x32_bf16 v[8:11], v[214:217], v[198:201], v[8:11]
	v_mfma_f32_16x16x32_bf16 v[64:67], v[210:213], v[154:157], v[64:67]
	v_mfma_f32_16x16x32_bf16 v[32:35], v[218:221], v[154:157], v[32:35]
	v_mfma_f32_16x16x32_bf16 v[56:59], v[210:213], v[170:173], v[56:59]
	v_mfma_f32_16x16x32_bf16 v[24:27], v[218:221], v[170:173], v[24:27]
	v_mfma_f32_16x16x32_bf16 v[48:51], v[210:213], v[194:197], v[48:51]
	v_mfma_f32_16x16x32_bf16 v[16:19], v[218:221], v[194:197], v[16:19]
	v_mfma_f32_16x16x32_bf16 v[40:43], v[210:213], v[202:205], v[40:43]
	v_mfma_f32_16x16x32_bf16 v[8:11], v[218:221], v[202:205], v[8:11]
	s_setprio 0
	s_cselect_b32 s89, s52, s58
	s_cselect_b32 s15, s53, s59
	s_add_u32 s84, s89, s14
	s_addc_u32 s85, s15, s64
	s_mov_b64 s[86:87], s[84:85]
	v_mov_b32_e32 v0, v160
	s_mov_b32 m0, s30
	s_waitcnt vmcnt(10)
	s_barrier
	ds_read_b128 v[150:153], v165 offset:16384
	ds_read_b128 v[154:157], v165 offset:17408
	ds_read_b128 v[166:169], v165 offset:18432
	ds_read_b128 v[170:173], v165 offset:19456
	ds_read_b128 v[190:193], v165 offset:20480
	ds_read_b128 v[194:197], v165 offset:21504
	ds_read_b128 v[198:201], v165 offset:22528
	ds_read_b128 v[202:205], v165 offset:23552
	s_nop 0
	global_load_lds_dwordx4 v0, s[86:87]
	v_mov_b32_e32 v0, v161
	s_mov_b32 m0, s31
	s_nop 0
	global_load_lds_dwordx4 v0, s[86:87]
	s_barrier
	s_waitcnt lgkmcnt(0)
	s_setprio 1
	s_waitcnt lgkmcnt(0)
	v_mfma_f32_16x16x32_bf16 v[124:127], v[132:135], v[150:153], v[124:127]
	v_mfma_f32_16x16x32_bf16 v[92:95], v[140:143], v[150:153], v[92:95]
	v_mfma_f32_16x16x32_bf16 v[116:119], v[132:135], v[166:169], v[116:119]
	v_mfma_f32_16x16x32_bf16 v[84:87], v[140:143], v[166:169], v[84:87]
	v_mfma_f32_16x16x32_bf16 v[108:111], v[132:135], v[190:193], v[108:111]
	v_mfma_f32_16x16x32_bf16 v[76:79], v[140:143], v[190:193], v[76:79]
	v_mfma_f32_16x16x32_bf16 v[100:103], v[132:135], v[198:201], v[100:103]
	v_mfma_f32_16x16x32_bf16 v[68:71], v[140:143], v[198:201], v[68:71]
	v_mfma_f32_16x16x32_bf16 v[124:127], v[136:139], v[154:157], v[124:127]
	v_mfma_f32_16x16x32_bf16 v[92:95], v[146:149], v[154:157], v[92:95]
	v_mfma_f32_16x16x32_bf16 v[116:119], v[136:139], v[170:173], v[116:119]
	v_mfma_f32_16x16x32_bf16 v[84:87], v[146:149], v[170:173], v[84:87]
	v_mfma_f32_16x16x32_bf16 v[108:111], v[136:139], v[194:197], v[108:111]
	v_mfma_f32_16x16x32_bf16 v[76:79], v[146:149], v[194:197], v[76:79]
	v_mfma_f32_16x16x32_bf16 v[100:103], v[136:139], v[202:205], v[100:103]
	v_mfma_f32_16x16x32_bf16 v[68:71], v[146:149], v[202:205], v[68:71]
	s_setprio 0
	s_barrier
	s_add_u32 s86, s66, s44
	s_addc_u32 s87, s67, s45
	v_mov_b32_e32 v0, v160
	s_add_i32 vcc_lo, vcc_lo, s17
	s_mov_b32 m0, vcc_lo
	s_nop 0
	global_load_lds_dwordx4 v0, s[86:87]
	v_mov_b32_e32 v0, v161
	s_add_i32 m0, vcc_lo, 0x2000
	s_nop 0
	global_load_lds_dwordx4 v0, s[86:87]
	s_barrier
	s_setprio 1
	v_mfma_f32_16x16x32_bf16 v[60:63], v[206:209], v[150:153], v[60:63]
	v_mfma_f32_16x16x32_bf16 v[28:31], v[214:217], v[150:153], v[28:31]
	v_mfma_f32_16x16x32_bf16 v[52:55], v[206:209], v[166:169], v[52:55]
	v_mfma_f32_16x16x32_bf16 v[20:23], v[214:217], v[166:169], v[20:23]
	v_mfma_f32_16x16x32_bf16 v[44:47], v[206:209], v[190:193], v[44:47]
	v_mfma_f32_16x16x32_bf16 v[12:15], v[214:217], v[190:193], v[12:15]
	v_mfma_f32_16x16x32_bf16 v[36:39], v[206:209], v[198:201], v[36:39]
	v_mfma_f32_16x16x32_bf16 v[4:7], v[214:217], v[198:201], v[4:7]
	v_mfma_f32_16x16x32_bf16 v[60:63], v[210:213], v[154:157], v[60:63]
	v_mfma_f32_16x16x32_bf16 v[28:31], v[218:221], v[154:157], v[28:31]
	v_mfma_f32_16x16x32_bf16 v[52:55], v[210:213], v[170:173], v[52:55]
	v_mfma_f32_16x16x32_bf16 v[20:23], v[218:221], v[170:173], v[20:23]
	v_mfma_f32_16x16x32_bf16 v[44:47], v[210:213], v[194:197], v[44:47]
	v_mfma_f32_16x16x32_bf16 v[12:15], v[218:221], v[194:197], v[12:15]
	v_mfma_f32_16x16x32_bf16 v[36:39], v[210:213], v[202:205], v[36:39]
	v_mfma_f32_16x16x32_bf16 v[4:7], v[218:221], v[202:205], v[4:7]
	s_setprio 0
	s_add_i32 vcc_lo, 0, 0x18000
	v_add_u32_e32 v0, vcc_lo, v163
	s_waitcnt vmcnt(10)
	s_barrier
	ds_read_b128 v[132:135], v0
	ds_read_b128 v[136:139], v0 offset:1024
	ds_read_b128 v[140:143], v0 offset:2048
	ds_read_b128 v[146:149], v0 offset:3072
	s_add_u32 s86, s89, s44
	s_addc_u32 s15, s15, s45
	s_add_u32 s86, s86, s14
	s_addc_u32 s87, s15, s64
	v_mov_b32_e32 v0, v160
	s_mov_b32 m0, s55
	ds_read_b128 v[150:153], v165 offset:32768
	ds_read_b128 v[154:157], v165 offset:33792
	ds_read_b128 v[166:169], v165 offset:34816
	ds_read_b128 v[170:173], v165 offset:35840
	ds_read_b128 v[190:193], v165 offset:36864
	ds_read_b128 v[194:197], v165 offset:37888
	ds_read_b128 v[198:201], v165 offset:38912
	ds_read_b128 v[202:205], v165 offset:39936
	s_nop 0
	global_load_lds_dwordx4 v0, s[86:87]
	v_mov_b32_e32 v0, v161
	s_mov_b32 m0, s69
	s_nop 0
	global_load_lds_dwordx4 v0, s[86:87]
	s_waitcnt lgkmcnt(8)
	s_barrier
	s_waitcnt lgkmcnt(0)
	s_setprio 1
	s_waitcnt lgkmcnt(0)
	v_mfma_f32_16x16x32_bf16 v[128:131], v[132:135], v[150:153], v[128:131]
	v_mfma_f32_16x16x32_bf16 v[96:99], v[140:143], v[150:153], v[96:99]
	v_mfma_f32_16x16x32_bf16 v[120:123], v[132:135], v[166:169], v[120:123]
	v_mfma_f32_16x16x32_bf16 v[88:91], v[140:143], v[166:169], v[88:91]
	v_mfma_f32_16x16x32_bf16 v[112:115], v[132:135], v[190:193], v[112:115]
	v_mfma_f32_16x16x32_bf16 v[80:83], v[140:143], v[190:193], v[80:83]
	v_mfma_f32_16x16x32_bf16 v[104:107], v[132:135], v[198:201], v[104:107]
	v_mfma_f32_16x16x32_bf16 v[72:75], v[140:143], v[198:201], v[72:75]
	v_mfma_f32_16x16x32_bf16 v[128:131], v[136:139], v[154:157], v[128:131]
	v_mfma_f32_16x16x32_bf16 v[96:99], v[146:149], v[154:157], v[96:99]
	v_mfma_f32_16x16x32_bf16 v[120:123], v[136:139], v[170:173], v[120:123]
	v_mfma_f32_16x16x32_bf16 v[88:91], v[146:149], v[170:173], v[88:91]
	v_mfma_f32_16x16x32_bf16 v[112:115], v[136:139], v[194:197], v[112:115]
	v_mfma_f32_16x16x32_bf16 v[80:83], v[146:149], v[194:197], v[80:83]
	v_mfma_f32_16x16x32_bf16 v[104:107], v[136:139], v[202:205], v[104:107]
	v_mfma_f32_16x16x32_bf16 v[72:75], v[146:149], v[202:205], v[72:75]
	s_setprio 0
	s_waitcnt vmcnt(10)
	s_barrier
	s_add_i32 s14, 0, 0x1c000
	s_add_u32 s66, s66, 0x80
	v_add_u32_e32 v0, s14, v163
	s_addc_u32 s67, s67, 0
	ds_read_b128 v[206:209], v0
	ds_read_b128 v[210:213], v0 offset:1024
	ds_read_b128 v[214:217], v0 offset:2048
	ds_read_b128 v[218:221], v0 offset:3072
	s_mov_b64 s[86:87], s[66:67]
	v_mov_b32_e32 v0, v160
	s_add_i32 s15, vcc_lo, s17
	s_mov_b32 m0, s15
	s_nop 0
	global_load_lds_dwordx4 v0, s[86:87]
	v_mov_b32_e32 v0, v161
	s_add_i32 m0, s15, 0x2000
	s_nop 0
	global_load_lds_dwordx4 v0, s[86:87]
	s_barrier
; #define PG8_STAGEA(bufoff, hh, kb, nx) do { if constexpr (Sched::GATHER) { unsigned _o[2]; _o[0] = (nx) ? vN[hh][0] : vC[hh][0]; _o[1] = (nx) ? vN[hh][1] : vC[hh][1]; PG8_STAGE(bufoff, cA + (kb), _o); } \
;         else { PG8_STAGE(bufoff, ((nx) ? nA : cA) + (hh) * hstep + (kb), voffA); } } while (0)
; template <class Epi, class Sched>
; __device__ __forceinline__ void gemm_phase(LAS unsigned char* lds, const int K_, const Sched& S, const Epi& E, const int wave_) {
;     ...
;         if (Epi::NSTORE > 0 && hoisted) { PG8_BODY(true); t = 2; }
;         for (; t < nt; t += 2) { PG8_BODY(false); }
;         hoisted = false;
;         if constexpr (Epi::NSTORE > 0) { if (has_next) { PG8_STAGEA(PG8_SA(1, 1), 1, kstep, true); hoisted = true; } }
	s_waitcnt lgkmcnt(0)
	s_setprio 1
	s_waitcnt lgkmcnt(0)
	v_mfma_f32_16x16x32_bf16 v[64:67], v[206:209], v[150:153], v[64:67]
	v_mfma_f32_16x16x32_bf16 v[32:35], v[214:217], v[150:153], v[32:35]
	v_mfma_f32_16x16x32_bf16 v[56:59], v[206:209], v[166:169], v[56:59]
	v_mfma_f32_16x16x32_bf16 v[24:27], v[214:217], v[166:169], v[24:27]
	v_mfma_f32_16x16x32_bf16 v[48:51], v[206:209], v[190:193], v[48:51]
	v_mfma_f32_16x16x32_bf16 v[16:19], v[214:217], v[190:193], v[16:19]
	v_mfma_f32_16x16x32_bf16 v[40:43], v[206:209], v[198:201], v[40:43]
	v_mfma_f32_16x16x32_bf16 v[8:11], v[214:217], v[198:201], v[8:11]
	v_mfma_f32_16x16x32_bf16 v[64:67], v[210:213], v[154:157], v[64:67]
	v_mfma_f32_16x16x32_bf16 v[32:35], v[218:221], v[154:157], v[32:35]
	v_mfma_f32_16x16x32_bf16 v[56:59], v[210:213], v[170:173], v[56:59]
	v_mfma_f32_16x16x32_bf16 v[24:27], v[218:221], v[170:173], v[24:27]
	v_mfma_f32_16x16x32_bf16 v[48:51], v[210:213], v[194:197], v[48:51]
	v_mfma_f32_16x16x32_bf16 v[16:19], v[218:221], v[194:197], v[16:19]
	v_mfma_f32_16x16x32_bf16 v[40:43], v[210:213], v[202:205], v[40:43]
	v_mfma_f32_16x16x32_bf16 v[8:11], v[218:221], v[202:205], v[8:11]
	s_setprio 0
	s_add_u32 s84, s84, 0x80
	s_addc_u32 s85, s85, 0
	v_mov_b32_e32 v0, v160
	s_mov_b32 m0, s71
	s_waitcnt vmcnt(10)
	s_barrier
	ds_read_b128 v[150:153], v165 offset:49152
	ds_read_b128 v[154:157], v165 offset:50176
	ds_read_b128 v[166:169], v165 offset:51200
	ds_read_b128 v[170:173], v165 offset:52224
	ds_read_b128 v[190:193], v165 offset:53248
	ds_read_b128 v[194:197], v165 offset:54272
	ds_read_b128 v[198:201], v165 offset:55296
	ds_read_b128 v[202:205], v165 offset:56320
	s_nop 0
	global_load_lds_dwordx4 v0, s[84:85]
	v_mov_b32_e32 v0, v161
	s_mov_b32 m0, s75
	s_nop 0
	global_load_lds_dwordx4 v0, s[84:85]
	s_barrier
	s_waitcnt lgkmcnt(0)
	s_setprio 1
	s_waitcnt lgkmcnt(0)
	v_mfma_f32_16x16x32_bf16 v[124:127], v[132:135], v[150:153], v[124:127]
	v_mfma_f32_16x16x32_bf16 v[92:95], v[140:143], v[150:153], v[92:95]
	v_mfma_f32_16x16x32_bf16 v[116:119], v[132:135], v[166:169], v[116:119]
	v_mfma_f32_16x16x32_bf16 v[84:87], v[140:143], v[166:169], v[84:87]
	v_mfma_f32_16x16x32_bf16 v[108:111], v[132:135], v[190:193], v[108:111]
	v_mfma_f32_16x16x32_bf16 v[76:79], v[140:143], v[190:193], v[76:79]
	v_mfma_f32_16x16x32_bf16 v[100:103], v[132:135], v[198:201], v[100:103]
	v_mfma_f32_16x16x32_bf16 v[68:71], v[140:143], v[198:201], v[68:71]
	v_mfma_f32_16x16x32_bf16 v[124:127], v[136:139], v[154:157], v[124:127]
	v_mfma_f32_16x16x32_bf16 v[92:95], v[146:149], v[154:157], v[92:95]
	v_mfma_f32_16x16x32_bf16 v[116:119], v[136:139], v[170:173], v[116:119]
	v_mfma_f32_16x16x32_bf16 v[84:87], v[146:149], v[170:173], v[84:87]
	v_mfma_f32_16x16x32_bf16 v[108:111], v[136:139], v[194:197], v[108:111]
	v_mfma_f32_16x16x32_bf16 v[76:79], v[146:149], v[194:197], v[76:79]
	v_mfma_f32_16x16x32_bf16 v[100:103], v[136:139], v[202:205], v[100:103]
	v_mfma_f32_16x16x32_bf16 v[68:71], v[146:149], v[202:205], v[68:71]
	s_setprio 0
	s_barrier
	s_add_u32 s66, s66, s44
	s_addc_u32 s67, s67, s45
	v_mov_b32_e32 v0, v160
	s_add_i32 s14, s14, s17
	s_mov_b32 m0, s14
	s_nop 0
	global_load_lds_dwordx4 v0, s[66:67]
	v_mov_b32_e32 v0, v161
	s_add_i32 m0, s14, 0x2000
	s_nop 0
	global_load_lds_dwordx4 v0, s[66:67]
	s_barrier
	s_setprio 1
	v_mfma_f32_16x16x32_bf16 v[60:63], v[206:209], v[150:153], v[60:63]
	v_mfma_f32_16x16x32_bf16 v[28:31], v[214:217], v[150:153], v[28:31]
	v_mfma_f32_16x16x32_bf16 v[52:55], v[206:209], v[166:169], v[52:55]
	v_mfma_f32_16x16x32_bf16 v[20:23], v[214:217], v[166:169], v[20:23]
	v_mfma_f32_16x16x32_bf16 v[44:47], v[206:209], v[190:193], v[44:47]
	v_mfma_f32_16x16x32_bf16 v[12:15], v[214:217], v[190:193], v[12:15]
	v_mfma_f32_16x16x32_bf16 v[36:39], v[206:209], v[198:201], v[36:39]
	v_mfma_f32_16x16x32_bf16 v[4:7], v[214:217], v[198:201], v[4:7]
	v_mfma_f32_16x16x32_bf16 v[60:63], v[210:213], v[154:157], v[60:63]
	v_mfma_f32_16x16x32_bf16 v[28:31], v[218:221], v[154:157], v[28:31]
	v_mfma_f32_16x16x32_bf16 v[52:55], v[210:213], v[170:173], v[52:55]
	v_mfma_f32_16x16x32_bf16 v[20:23], v[218:221], v[170:173], v[20:23]
	v_mfma_f32_16x16x32_bf16 v[44:47], v[210:213], v[194:197], v[44:47]
	v_mfma_f32_16x16x32_bf16 v[12:15], v[218:221], v[194:197], v[12:15]
	v_mfma_f32_16x16x32_bf16 v[36:39], v[210:213], v[202:205], v[36:39]
	v_mfma_f32_16x16x32_bf16 v[4:7], v[218:221], v[202:205], v[4:7]
	s_setprio 0
	s_add_u32 s24, s24, 0x100
	s_addc_u32 s25, s25, 0
	s_cmp_lt_i32 s51, s70
	s_mov_b32 s64, s51
	s_waitcnt vmcnt(10)
	s_barrier
	s_cbranch_scc1 .LBB0_1242
	s_waitcnt vmcnt(6)
	s_mov_b32 s89, s18
	s_mov_b32 s19, s68
	s_mov_b32 s68, s22
	s_mov_b32 s18, s23
	s_mov_b32 s23, s38
	v_readlane_b32 s38, v254, 62

.LBB0_1556:
	s_cmp_eq_u32 s58, s10
	s_cselect_b64 vcc, -1, 0
	s_add_i32 s10, s10, 2
	s_add_u32 s14, s4, s20
	s_addc_u32 s15, s5, s21
	s_and_b64 s[24:25], vcc, exec
	s_cselect_b32 s25, s45, s15
	s_cselect_b32 s24, s44, s14
	s_add_i32 s14, 0, 0x10000
	v_add_u32_e32 v0, s14, v150
	s_waitcnt lgkmcnt(0)
	ds_read_b128 v[132:135], v0
	ds_read_b128 v[158:161], v0 offset:1024
	ds_read_b128 v[162:165], v0 offset:2048
	ds_read_b128 v[166:169], v0 offset:3072
	s_and_b64 s[30:31], vcc, exec
	s_cselect_b32 s15, 0, s21
	s_cselect_b32 s29, 0, s20
	s_add_u32 s30, s76, s20
	s_addc_u32 s31, s77, s21
	s_add_u32 s30, s30, 0xffffff80
	s_addc_u32 s31, s31, -1
	v_mov_b32_e32 v0, v146
	ds_read_b128 v[170:173], v152
	ds_read_b128 v[190:193], v152 offset:1024
	ds_read_b128 v[194:197], v152 offset:2048
	ds_read_b128 v[198:201], v152 offset:3072
	ds_read_b128 v[202:205], v152 offset:4096
	ds_read_b128 v[206:209], v152 offset:5120
	ds_read_b128 v[210:213], v152 offset:6144
	ds_read_b128 v[214:217], v152 offset:7168
	s_add_i32 m0, s27, 0xc000
	s_nop 0
	global_load_lds_dwordx4 v0, s[30:31]
	v_mov_b32_e32 v0, v148
	s_add_i32 m0, s27, 0xe000
	s_nop 0
	global_load_lds_dwordx4 v0, s[30:31]
	s_waitcnt lgkmcnt(8)
	s_barrier
	s_waitcnt lgkmcnt(0)
	s_setprio 1
	s_waitcnt lgkmcnt(0)
	v_mfma_f32_16x16x32_bf16 v[4:7], v[132:135], v[170:173], v[4:7]
	v_mfma_f32_16x16x32_bf16 v[8:11], v[162:165], v[170:173], v[8:11]
	v_mfma_f32_16x16x32_bf16 v[12:15], v[132:135], v[194:197], v[12:15]
	v_mfma_f32_16x16x32_bf16 v[16:19], v[162:165], v[194:197], v[16:19]
	v_mfma_f32_16x16x32_bf16 v[20:23], v[132:135], v[202:205], v[20:23]
	v_mfma_f32_16x16x32_bf16 v[24:27], v[162:165], v[202:205], v[24:27]
	v_mfma_f32_16x16x32_bf16 v[28:31], v[132:135], v[210:213], v[28:31]
	v_mfma_f32_16x16x32_bf16 v[32:35], v[162:165], v[210:213], v[32:35]
	v_mfma_f32_16x16x32_bf16 v[4:7], v[158:161], v[190:193], v[4:7]
	v_mfma_f32_16x16x32_bf16 v[8:11], v[166:169], v[190:193], v[8:11]
	v_mfma_f32_16x16x32_bf16 v[12:15], v[158:161], v[198:201], v[12:15]
	v_mfma_f32_16x16x32_bf16 v[16:19], v[166:169], v[198:201], v[16:19]
	v_mfma_f32_16x16x32_bf16 v[20:23], v[158:161], v[206:209], v[20:23]
	v_mfma_f32_16x16x32_bf16 v[24:27], v[166:169], v[206:209], v[24:27]
	v_mfma_f32_16x16x32_bf16 v[28:31], v[158:161], v[214:217], v[28:31]
	v_mfma_f32_16x16x32_bf16 v[32:35], v[166:169], v[214:217], v[32:35]
	s_setprio 0
	s_waitcnt vmcnt(10)
	s_barrier
	s_add_i32 s47, 0, 0x14000
	v_add_u32_e32 v0, s47, v150
	ds_read_b128 v[218:221], v0
	ds_read_b128 v[222:225], v0 offset:1024
	ds_read_b128 v[226:229], v0 offset:2048
	ds_read_b128 v[230:233], v0 offset:3072
	s_mov_b64 s[30:31], s[24:25]
	v_mov_b32_e32 v0, v142
	s_add_i32 s14, s14, s26
	s_mov_b32 m0, s14
	s_nop 0
	global_load_lds_dwordx4 v0, s[30:31]
	v_mov_b32_e32 v0, v143
	s_add_i32 m0, s14, 0x2000
	s_nop 0
	global_load_lds_dwordx4 v0, s[30:31]
	s_barrier
	s_waitcnt lgkmcnt(0)
	s_setprio 1
	s_waitcnt lgkmcnt(0)
	v_mfma_f32_16x16x32_bf16 v[40:43], v[218:221], v[170:173], v[40:43]
	v_mfma_f32_16x16x32_bf16 v[44:47], v[226:229], v[170:173], v[44:47]
	v_mfma_f32_16x16x32_bf16 v[48:51], v[218:221], v[194:197], v[48:51]
	v_mfma_f32_16x16x32_bf16 v[52:55], v[226:229], v[194:197], v[52:55]
	v_mfma_f32_16x16x32_bf16 v[56:59], v[218:221], v[202:205], v[56:59]
	v_mfma_f32_16x16x32_bf16 v[60:63], v[226:229], v[202:205], v[60:63]
	v_mfma_f32_16x16x32_bf16 v[68:71], v[218:221], v[210:213], v[68:71]
	v_mfma_f32_16x16x32_bf16 v[76:79], v[226:229], v[210:213], v[76:79]
	v_mfma_f32_16x16x32_bf16 v[40:43], v[222:225], v[190:193], v[40:43]
	v_mfma_f32_16x16x32_bf16 v[44:47], v[230:233], v[190:193], v[44:47]
	v_mfma_f32_16x16x32_bf16 v[48:51], v[222:225], v[198:201], v[48:51]
	v_mfma_f32_16x16x32_bf16 v[52:55], v[230:233], v[198:201], v[52:55]
	v_mfma_f32_16x16x32_bf16 v[56:59], v[222:225], v[206:209], v[56:59]
	v_mfma_f32_16x16x32_bf16 v[60:63], v[230:233], v[206:209], v[60:63]
	v_mfma_f32_16x16x32_bf16 v[68:71], v[222:225], v[214:217], v[68:71]
	v_mfma_f32_16x16x32_bf16 v[76:79], v[230:233], v[214:217], v[76:79]
	s_setprio 0
	s_add_u32 s50, s76, s29
	v_cndmask_b32_e32 v0, v147, v153, vcc
	s_addc_u32 s51, s77, s15
	s_mov_b64 s[30:31], s[50:51]
	v_mov_b32_e32 v157, v0
	s_mov_b32 m0, s27
	s_waitcnt vmcnt(10)
	s_barrier
	ds_read_b128 v[170:173], v152 offset:16384
	ds_read_b128 v[190:193], v152 offset:17408
	ds_read_b128 v[194:197], v152 offset:18432
	ds_read_b128 v[198:201], v152 offset:19456
	ds_read_b128 v[202:205], v152 offset:20480
	ds_read_b128 v[206:209], v152 offset:21504
	ds_read_b128 v[210:213], v152 offset:22528
	ds_read_b128 v[214:217], v152 offset:23552
	v_cndmask_b32_e32 v1, v145, v154, vcc
	s_nop 0
	global_load_lds_dwordx4 v157, s[30:31]
	v_mov_b32_e32 v157, v1
	s_mov_b32 m0, s52
	s_nop 0
	global_load_lds_dwordx4 v157, s[30:31]
	s_barrier
	s_waitcnt lgkmcnt(0)
	s_setprio 1
	s_waitcnt lgkmcnt(0)
	v_mfma_f32_16x16x32_bf16 v[64:67], v[132:135], v[170:173], v[64:67]
	v_mfma_f32_16x16x32_bf16 v[72:75], v[162:165], v[170:173], v[72:75]
	v_mfma_f32_16x16x32_bf16 v[80:83], v[132:135], v[194:197], v[80:83]
	v_mfma_f32_16x16x32_bf16 v[84:87], v[162:165], v[194:197], v[84:87]
	v_mfma_f32_16x16x32_bf16 v[88:91], v[132:135], v[202:205], v[88:91]
	v_mfma_f32_16x16x32_bf16 v[92:95], v[162:165], v[202:205], v[92:95]
	v_mfma_f32_16x16x32_bf16 v[96:99], v[132:135], v[210:213], v[96:99]
	v_mfma_f32_16x16x32_bf16 v[100:103], v[162:165], v[210:213], v[100:103]
	v_mfma_f32_16x16x32_bf16 v[64:67], v[158:161], v[190:193], v[64:67]
	v_mfma_f32_16x16x32_bf16 v[72:75], v[166:169], v[190:193], v[72:75]
	v_mfma_f32_16x16x32_bf16 v[80:83], v[158:161], v[198:201], v[80:83]
	v_mfma_f32_16x16x32_bf16 v[84:87], v[166:169], v[198:201], v[84:87]
	v_mfma_f32_16x16x32_bf16 v[88:91], v[158:161], v[206:209], v[88:91]
	v_mfma_f32_16x16x32_bf16 v[92:95], v[166:169], v[206:209], v[92:95]
	v_mfma_f32_16x16x32_bf16 v[96:99], v[158:161], v[214:217], v[96:99]
	v_mfma_f32_16x16x32_bf16 v[100:103], v[166:169], v[214:217], v[100:103]
	s_setprio 0
	s_barrier
	s_add_u32 s30, s24, s0
	s_addc_u32 s31, s25, s1
	v_mov_b32_e32 v132, v142
	s_add_i32 s14, s47, s26
	s_mov_b32 m0, s14
	s_nop 0
	global_load_lds_dwordx4 v132, s[30:31]
	v_mov_b32_e32 v132, v143
	s_add_i32 m0, s14, 0x2000
	s_nop 0
	global_load_lds_dwordx4 v132, s[30:31]
	s_barrier
	s_setprio 1
	v_mfma_f32_16x16x32_bf16 v[104:107], v[218:221], v[170:173], v[104:107]
	v_mfma_f32_16x16x32_bf16 v[108:111], v[226:229], v[170:173], v[108:111]
	v_mfma_f32_16x16x32_bf16 v[112:115], v[218:221], v[194:197], v[112:115]
	v_mfma_f32_16x16x32_bf16 v[116:119], v[226:229], v[194:197], v[116:119]
	v_mfma_f32_16x16x32_bf16 v[120:123], v[218:221], v[202:205], v[120:123]
	v_mfma_f32_16x16x32_bf16 v[124:127], v[226:229], v[202:205], v[124:127]
	v_mfma_f32_16x16x32_bf16 v[128:131], v[218:221], v[210:213], v[128:131]
	v_mfma_f32_16x16x32_bf16 v[36:39], v[226:229], v[210:213], v[36:39]
	v_mfma_f32_16x16x32_bf16 v[104:107], v[222:225], v[190:193], v[104:107]
	v_mfma_f32_16x16x32_bf16 v[108:111], v[230:233], v[190:193], v[108:111]
	v_mfma_f32_16x16x32_bf16 v[112:115], v[222:225], v[198:201], v[112:115]
	v_mfma_f32_16x16x32_bf16 v[116:119], v[230:233], v[198:201], v[116:119]
	v_mfma_f32_16x16x32_bf16 v[120:123], v[222:225], v[206:209], v[120:123]
	v_mfma_f32_16x16x32_bf16 v[124:127], v[230:233], v[206:209], v[124:127]
	v_mfma_f32_16x16x32_bf16 v[128:131], v[222:225], v[214:217], v[128:131]
	v_mfma_f32_16x16x32_bf16 v[36:39], v[230:233], v[214:217], v[36:39]
	s_setprio 0
	s_add_i32 s14, 0, 0x18000
	v_add_u32_e32 v157, s14, v150
	s_waitcnt vmcnt(10)
	s_barrier
	ds_read_b128 v[132:135], v157
	ds_read_b128 v[158:161], v157 offset:1024
	ds_read_b128 v[162:165], v157 offset:2048
	ds_read_b128 v[166:169], v157 offset:3072
	s_mov_b32 m0, s53
	v_cndmask_b32_e32 v157, v146, v155, vcc
	s_mov_b64 s[30:31], s[50:51]
	ds_read_b128 v[170:173], v152 offset:32768
	ds_read_b128 v[190:193], v152 offset:33792
	ds_read_b128 v[194:197], v152 offset:34816
	ds_read_b128 v[198:201], v152 offset:35840
	ds_read_b128 v[202:205], v152 offset:36864
	ds_read_b128 v[206:209], v152 offset:37888
	ds_read_b128 v[210:213], v152 offset:38912
	ds_read_b128 v[214:217], v152 offset:39936
	v_cndmask_b32_e32 v182, v148, v156, vcc
	s_nop 0
	global_load_lds_dwordx4 v157, s[30:31]
	s_mov_b32 m0, s54
	s_nop 0
	global_load_lds_dwordx4 v182, s[30:31]
	s_waitcnt lgkmcnt(8)
	s_barrier
	s_waitcnt lgkmcnt(0)
	s_setprio 1
	s_waitcnt lgkmcnt(0)
	v_mfma_f32_16x16x32_bf16 v[4:7], v[132:135], v[170:173], v[4:7]
	v_mfma_f32_16x16x32_bf16 v[8:11], v[162:165], v[170:173], v[8:11]
	v_mfma_f32_16x16x32_bf16 v[12:15], v[132:135], v[194:197], v[12:15]
	v_mfma_f32_16x16x32_bf16 v[16:19], v[162:165], v[194:197], v[16:19]
	v_mfma_f32_16x16x32_bf16 v[20:23], v[132:135], v[202:205], v[20:23]
	v_mfma_f32_16x16x32_bf16 v[24:27], v[162:165], v[202:205], v[24:27]
	v_mfma_f32_16x16x32_bf16 v[28:31], v[132:135], v[210:213], v[28:31]
	v_mfma_f32_16x16x32_bf16 v[32:35], v[162:165], v[210:213], v[32:35]
	v_mfma_f32_16x16x32_bf16 v[4:7], v[158:161], v[190:193], v[4:7]
	v_mfma_f32_16x16x32_bf16 v[8:11], v[166:169], v[190:193], v[8:11]
	v_mfma_f32_16x16x32_bf16 v[12:15], v[158:161], v[198:201], v[12:15]
	v_mfma_f32_16x16x32_bf16 v[16:19], v[166:169], v[198:201], v[16:19]
	v_mfma_f32_16x16x32_bf16 v[20:23], v[158:161], v[206:209], v[20:23]
	v_mfma_f32_16x16x32_bf16 v[24:27], v[166:169], v[206:209], v[24:27]
	v_mfma_f32_16x16x32_bf16 v[28:31], v[158:161], v[214:217], v[28:31]
	v_mfma_f32_16x16x32_bf16 v[32:35], v[166:169], v[214:217], v[32:35]
	s_setprio 0
	s_waitcnt vmcnt(10)
	s_barrier
	s_add_i32 s15, 0, 0x1c000
	s_add_u32 s24, s24, 0x80
	v_add_u32_e32 v157, s15, v150
	s_addc_u32 s25, s25, 0
	ds_read_b128 v[218:221], v157
	ds_read_b128 v[222:225], v157 offset:1024
	ds_read_b128 v[226:229], v157 offset:2048
	ds_read_b128 v[230:233], v157 offset:3072
	s_mov_b64 s[30:31], s[24:25]
	v_mov_b32_e32 v157, v142
	s_add_i32 s14, s14, s26
	s_mov_b32 m0, s14
	s_nop 0
	global_load_lds_dwordx4 v157, s[30:31]
	v_mov_b32_e32 v157, v143
	s_add_i32 m0, s14, 0x2000
	s_nop 0
	global_load_lds_dwordx4 v157, s[30:31]
	s_barrier
; template <class Epi, class Sched>
; __device__ __forceinline__ void gemm_phase(LAS unsigned char* lds, const int K_, const Sched& S, const Epi& E, const int wave_) {
;     ...
;         for (; t < nt; t += 2) { PG8_BODY(false); }
	s_waitcnt lgkmcnt(0)
	s_setprio 1
	s_waitcnt lgkmcnt(0)
	v_mfma_f32_16x16x32_bf16 v[40:43], v[218:221], v[170:173], v[40:43]
	v_mfma_f32_16x16x32_bf16 v[44:47], v[226:229], v[170:173], v[44:47]
	v_mfma_f32_16x16x32_bf16 v[48:51], v[218:221], v[194:197], v[48:51]
	v_mfma_f32_16x16x32_bf16 v[52:55], v[226:229], v[194:197], v[52:55]
	v_mfma_f32_16x16x32_bf16 v[56:59], v[218:221], v[202:205], v[56:59]
	v_mfma_f32_16x16x32_bf16 v[60:63], v[226:229], v[202:205], v[60:63]
	v_mfma_f32_16x16x32_bf16 v[68:71], v[218:221], v[210:213], v[68:71]
	v_mfma_f32_16x16x32_bf16 v[76:79], v[226:229], v[210:213], v[76:79]
	v_mfma_f32_16x16x32_bf16 v[40:43], v[222:225], v[190:193], v[40:43]
	v_mfma_f32_16x16x32_bf16 v[44:47], v[230:233], v[190:193], v[44:47]
	v_mfma_f32_16x16x32_bf16 v[48:51], v[222:225], v[198:201], v[48:51]
	v_mfma_f32_16x16x32_bf16 v[52:55], v[230:233], v[198:201], v[52:55]
	v_mfma_f32_16x16x32_bf16 v[56:59], v[222:225], v[206:209], v[56:59]
	v_mfma_f32_16x16x32_bf16 v[60:63], v[230:233], v[206:209], v[60:63]
	v_mfma_f32_16x16x32_bf16 v[68:71], v[222:225], v[214:217], v[68:71]
	v_mfma_f32_16x16x32_bf16 v[76:79], v[230:233], v[214:217], v[76:79]
	s_setprio 0
	s_add_u32 s30, s50, 0x80
	s_addc_u32 s31, s51, 0
	s_mov_b32 m0, s56
	s_waitcnt vmcnt(10)
	s_barrier
	ds_read_b128 v[170:173], v152 offset:49152
	ds_read_b128 v[190:193], v152 offset:50176
	ds_read_b128 v[194:197], v152 offset:51200
	ds_read_b128 v[198:201], v152 offset:52224
	ds_read_b128 v[202:205], v152 offset:53248
	ds_read_b128 v[206:209], v152 offset:54272
	ds_read_b128 v[210:213], v152 offset:55296
	ds_read_b128 v[214:217], v152 offset:56320
	s_nop 0
	global_load_lds_dwordx4 v0, s[30:31]
	s_mov_b32 m0, s57
	s_nop 0
	global_load_lds_dwordx4 v1, s[30:31]
	s_barrier
	s_waitcnt lgkmcnt(0)
	s_setprio 1
	s_waitcnt lgkmcnt(0)
	v_mfma_f32_16x16x32_bf16 v[64:67], v[132:135], v[170:173], v[64:67]
	v_mfma_f32_16x16x32_bf16 v[72:75], v[162:165], v[170:173], v[72:75]
	v_mfma_f32_16x16x32_bf16 v[80:83], v[132:135], v[194:197], v[80:83]
	v_mfma_f32_16x16x32_bf16 v[84:87], v[162:165], v[194:197], v[84:87]
	v_mfma_f32_16x16x32_bf16 v[88:91], v[132:135], v[202:205], v[88:91]
	v_mfma_f32_16x16x32_bf16 v[92:95], v[162:165], v[202:205], v[92:95]
	v_mfma_f32_16x16x32_bf16 v[96:99], v[132:135], v[210:213], v[96:99]
	v_mfma_f32_16x16x32_bf16 v[100:103], v[162:165], v[210:213], v[100:103]
	v_mfma_f32_16x16x32_bf16 v[64:67], v[158:161], v[190:193], v[64:67]
	v_mfma_f32_16x16x32_bf16 v[72:75], v[166:169], v[190:193], v[72:75]
	v_mfma_f32_16x16x32_bf16 v[80:83], v[158:161], v[198:201], v[80:83]
	v_mfma_f32_16x16x32_bf16 v[84:87], v[166:169], v[198:201], v[84:87]
	v_mfma_f32_16x16x32_bf16 v[88:91], v[158:161], v[206:209], v[88:91]
	v_mfma_f32_16x16x32_bf16 v[92:95], v[166:169], v[206:209], v[92:95]
	v_mfma_f32_16x16x32_bf16 v[96:99], v[158:161], v[214:217], v[96:99]
	v_mfma_f32_16x16x32_bf16 v[100:103], v[166:169], v[214:217], v[100:103]
	s_setprio 0
	s_barrier
	s_add_u32 s24, s24, s0
	s_addc_u32 s25, s25, s1
	v_mov_b32_e32 v0, v142
	s_add_i32 s14, s15, s26
	s_mov_b32 m0, s14
	s_nop 0
	global_load_lds_dwordx4 v0, s[24:25]
	v_mov_b32_e32 v0, v143
	s_add_i32 m0, s14, 0x2000
	s_nop 0
	global_load_lds_dwordx4 v0, s[24:25]
	s_barrier
	s_setprio 1
	v_mfma_f32_16x16x32_bf16 v[104:107], v[218:221], v[170:173], v[104:107]
	v_mfma_f32_16x16x32_bf16 v[108:111], v[226:229], v[170:173], v[108:111]
	v_mfma_f32_16x16x32_bf16 v[112:115], v[218:221], v[194:197], v[112:115]
	v_mfma_f32_16x16x32_bf16 v[116:119], v[226:229], v[194:197], v[116:119]
	v_mfma_f32_16x16x32_bf16 v[120:123], v[218:221], v[202:205], v[120:123]
	v_mfma_f32_16x16x32_bf16 v[124:127], v[226:229], v[202:205], v[124:127]
	v_mfma_f32_16x16x32_bf16 v[128:131], v[218:221], v[210:213], v[128:131]
	v_mfma_f32_16x16x32_bf16 v[36:39], v[226:229], v[210:213], v[36:39]
	v_mfma_f32_16x16x32_bf16 v[104:107], v[222:225], v[190:193], v[104:107]
	v_mfma_f32_16x16x32_bf16 v[108:111], v[230:233], v[190:193], v[108:111]
	v_mfma_f32_16x16x32_bf16 v[112:115], v[222:225], v[198:201], v[112:115]
	v_mfma_f32_16x16x32_bf16 v[116:119], v[230:233], v[198:201], v[116:119]
	v_mfma_f32_16x16x32_bf16 v[120:123], v[222:225], v[206:209], v[120:123]
	v_mfma_f32_16x16x32_bf16 v[124:127], v[230:233], v[206:209], v[124:127]
	v_mfma_f32_16x16x32_bf16 v[128:131], v[222:225], v[214:217], v[128:131]
	v_mfma_f32_16x16x32_bf16 v[36:39], v[230:233], v[214:217], v[36:39]
	s_setprio 0
	s_add_u32 s20, s20, 0x100
	s_addc_u32 s21, s21, 0
	s_cmp_lt_i32 s10, s55
	s_waitcnt vmcnt(10)
	s_barrier
	s_cbranch_scc1 .LBB0_1556
	s_waitcnt vmcnt(6)

.LBB0_1628:
	s_add_i32 s31, s24, 2
	s_add_u32 s14, s46, s29
	s_addc_u32 s15, s47, s30
	s_add_i32 s25, 0, 0x10000
	v_add_u32_e32 v0, s25, v137
	s_add_u32 s39, s9, s29
	ds_read_b128 v[140:143], v0
	ds_read_b128 v[146:149], v0 offset:1024
	ds_read_b128 v[150:153], v0 offset:2048
	ds_read_b128 v[154:157], v0 offset:3072
	s_addc_u32 s51, s21, s30
	s_add_u32 s50, s39, 0xffffff80
	s_addc_u32 s51, s51, -1
	s_add_i32 s66, s25, s17
	s_add_i32 m0, s26, 0xc000
	s_add_i32 s39, s26, 0xe000
	s_add_i32 s64, 0, 0x14000
	s_add_i32 s67, s66, 0x2000
	s_cmp_eq_u32 s59, s24
	s_cselect_b32 s24, s42, s14
	s_cselect_b32 s25, s43, s15
	s_cselect_b32 s14, 0, s30
	s_cselect_b32 s15, 0, s29
	v_mov_b32_e32 v0, v132
	ds_read_b128 v[158:161], v139
	ds_read_b128 v[162:165], v139 offset:1024
	ds_read_b128 v[166:169], v139 offset:2048
	ds_read_b128 v[170:173], v139 offset:3072
	ds_read_b128 v[190:193], v139 offset:4096
	ds_read_b128 v[194:197], v139 offset:5120
	ds_read_b128 v[198:201], v139 offset:6144
	ds_read_b128 v[202:205], v139 offset:7168
	s_nop 0
	global_load_lds_dwordx4 v0, s[50:51]
	v_mov_b32_e32 v0, v134
	s_mov_b32 m0, s39
	s_nop 0
	global_load_lds_dwordx4 v0, s[50:51]
	s_waitcnt lgkmcnt(8)
	s_barrier
	s_waitcnt lgkmcnt(0)
	s_setprio 1
	s_waitcnt lgkmcnt(0)
	v_mfma_f32_16x16x32_bf16 v[128:131], v[140:143], v[158:161], v[128:131]
	v_mfma_f32_16x16x32_bf16 v[124:127], v[150:153], v[158:161], v[124:127]
	v_mfma_f32_16x16x32_bf16 v[112:115], v[140:143], v[166:169], v[112:115]
	v_mfma_f32_16x16x32_bf16 v[108:111], v[150:153], v[166:169], v[108:111]
	v_mfma_f32_16x16x32_bf16 v[96:99], v[140:143], v[190:193], v[96:99]
	v_mfma_f32_16x16x32_bf16 v[92:95], v[150:153], v[190:193], v[92:95]
	v_mfma_f32_16x16x32_bf16 v[80:83], v[140:143], v[198:201], v[80:83]
	v_mfma_f32_16x16x32_bf16 v[76:79], v[150:153], v[198:201], v[76:79]
	v_mfma_f32_16x16x32_bf16 v[128:131], v[146:149], v[162:165], v[128:131]
	v_mfma_f32_16x16x32_bf16 v[124:127], v[154:157], v[162:165], v[124:127]
	v_mfma_f32_16x16x32_bf16 v[112:115], v[146:149], v[170:173], v[112:115]
	v_mfma_f32_16x16x32_bf16 v[108:111], v[154:157], v[170:173], v[108:111]
	v_mfma_f32_16x16x32_bf16 v[96:99], v[146:149], v[194:197], v[96:99]
	v_mfma_f32_16x16x32_bf16 v[92:95], v[154:157], v[194:197], v[92:95]
	v_mfma_f32_16x16x32_bf16 v[80:83], v[146:149], v[202:205], v[80:83]
	v_mfma_f32_16x16x32_bf16 v[76:79], v[154:157], v[202:205], v[76:79]
	s_setprio 0
	s_waitcnt vmcnt(10)
	s_barrier
	v_add_u32_e32 v0, s64, v137
	ds_read_b128 v[206:209], v0
	ds_read_b128 v[210:213], v0 offset:1024
	ds_read_b128 v[214:217], v0 offset:2048
	ds_read_b128 v[218:221], v0 offset:3072
	s_mov_b64 s[50:51], s[24:25]
	v_mov_b32_e32 v0, v133
	s_mov_b32 m0, s66
	s_nop 0
	global_load_lds_dwordx4 v0, s[50:51]
	v_mov_b32_e32 v0, v135
	s_mov_b32 m0, s67
	s_nop 0
	global_load_lds_dwordx4 v0, s[50:51]
	s_barrier
	s_waitcnt lgkmcnt(0)
	s_setprio 1
	s_waitcnt lgkmcnt(0)
	v_mfma_f32_16x16x32_bf16 v[120:123], v[206:209], v[158:161], v[120:123]
	v_mfma_f32_16x16x32_bf16 v[116:119], v[214:217], v[158:161], v[116:119]
	v_mfma_f32_16x16x32_bf16 v[104:107], v[206:209], v[166:169], v[104:107]
	v_mfma_f32_16x16x32_bf16 v[100:103], v[214:217], v[166:169], v[100:103]
	v_mfma_f32_16x16x32_bf16 v[88:91], v[206:209], v[190:193], v[88:91]
	v_mfma_f32_16x16x32_bf16 v[84:87], v[214:217], v[190:193], v[84:87]
	v_mfma_f32_16x16x32_bf16 v[72:75], v[206:209], v[198:201], v[72:75]
	v_mfma_f32_16x16x32_bf16 v[68:71], v[214:217], v[198:201], v[68:71]
	v_mfma_f32_16x16x32_bf16 v[120:123], v[210:213], v[162:165], v[120:123]
	v_mfma_f32_16x16x32_bf16 v[116:119], v[218:221], v[162:165], v[116:119]
	v_mfma_f32_16x16x32_bf16 v[104:107], v[210:213], v[170:173], v[104:107]
	v_mfma_f32_16x16x32_bf16 v[100:103], v[218:221], v[170:173], v[100:103]
	v_mfma_f32_16x16x32_bf16 v[88:91], v[210:213], v[194:197], v[88:91]
	v_mfma_f32_16x16x32_bf16 v[84:87], v[218:221], v[194:197], v[84:87]
	v_mfma_f32_16x16x32_bf16 v[72:75], v[210:213], v[202:205], v[72:75]
	v_mfma_f32_16x16x32_bf16 v[68:71], v[218:221], v[202:205], v[68:71]
	s_setprio 0
	s_cselect_b32 s69, s44, s48
	s_cselect_b32 s39, s45, s49
	s_add_u32 s50, s69, s15
	s_addc_u32 s51, s39, s14
	s_mov_b64 s[66:67], s[50:51]
	v_mov_b32_e32 v0, v132
	s_mov_b32 m0, s26
	s_waitcnt vmcnt(10)
	s_barrier
	ds_read_b128 v[158:161], v139 offset:16384
	ds_read_b128 v[162:165], v139 offset:17408
	ds_read_b128 v[166:169], v139 offset:18432
	ds_read_b128 v[170:173], v139 offset:19456
	ds_read_b128 v[190:193], v139 offset:20480
	ds_read_b128 v[194:197], v139 offset:21504
	ds_read_b128 v[198:201], v139 offset:22528
	ds_read_b128 v[202:205], v139 offset:23552
	s_nop 0
	global_load_lds_dwordx4 v0, s[66:67]
	v_mov_b32_e32 v0, v134
	s_mov_b32 m0, s27
	s_nop 0
	global_load_lds_dwordx4 v0, s[66:67]
	s_barrier
	s_waitcnt lgkmcnt(0)
	s_setprio 1
	s_waitcnt lgkmcnt(0)
	v_mfma_f32_16x16x32_bf16 v[64:67], v[140:143], v[158:161], v[64:67]
	v_mfma_f32_16x16x32_bf16 v[60:63], v[150:153], v[158:161], v[60:63]
	v_mfma_f32_16x16x32_bf16 v[48:51], v[140:143], v[166:169], v[48:51]
	v_mfma_f32_16x16x32_bf16 v[44:47], v[150:153], v[166:169], v[44:47]
	v_mfma_f32_16x16x32_bf16 v[32:35], v[140:143], v[190:193], v[32:35]
	v_mfma_f32_16x16x32_bf16 v[28:31], v[150:153], v[190:193], v[28:31]
	v_mfma_f32_16x16x32_bf16 v[16:19], v[140:143], v[198:201], v[16:19]
	v_mfma_f32_16x16x32_bf16 v[12:15], v[150:153], v[198:201], v[12:15]
	v_mfma_f32_16x16x32_bf16 v[64:67], v[146:149], v[162:165], v[64:67]
	v_mfma_f32_16x16x32_bf16 v[60:63], v[154:157], v[162:165], v[60:63]
	v_mfma_f32_16x16x32_bf16 v[48:51], v[146:149], v[170:173], v[48:51]
	v_mfma_f32_16x16x32_bf16 v[44:47], v[154:157], v[170:173], v[44:47]
	v_mfma_f32_16x16x32_bf16 v[32:35], v[146:149], v[194:197], v[32:35]
	v_mfma_f32_16x16x32_bf16 v[28:31], v[154:157], v[194:197], v[28:31]
	v_mfma_f32_16x16x32_bf16 v[16:19], v[146:149], v[202:205], v[16:19]
	v_mfma_f32_16x16x32_bf16 v[12:15], v[154:157], v[202:205], v[12:15]
	s_setprio 0
	s_barrier
	s_add_u32 s66, s24, s4
	s_addc_u32 s67, s25, s5
	v_mov_b32_e32 v0, v133
	s_add_i32 s64, s64, s17
	s_mov_b32 m0, s64
	s_nop 0
	global_load_lds_dwordx4 v0, s[66:67]
	v_mov_b32_e32 v0, v135
	s_add_i32 m0, s64, 0x2000
	s_nop 0
	global_load_lds_dwordx4 v0, s[66:67]
	s_barrier
	s_setprio 1
	v_mfma_f32_16x16x32_bf16 v[56:59], v[206:209], v[158:161], v[56:59]
	v_mfma_f32_16x16x32_bf16 v[52:55], v[214:217], v[158:161], v[52:55]
	v_mfma_f32_16x16x32_bf16 v[40:43], v[206:209], v[166:169], v[40:43]
	v_mfma_f32_16x16x32_bf16 v[36:39], v[214:217], v[166:169], v[36:39]
	v_mfma_f32_16x16x32_bf16 v[24:27], v[206:209], v[190:193], v[24:27]
	v_mfma_f32_16x16x32_bf16 v[20:23], v[214:217], v[190:193], v[20:23]
	v_mfma_f32_16x16x32_bf16 v[8:11], v[206:209], v[198:201], v[8:11]
	v_mfma_f32_16x16x32_bf16 v[4:7], v[214:217], v[198:201], v[4:7]
	v_mfma_f32_16x16x32_bf16 v[56:59], v[210:213], v[162:165], v[56:59]
	v_mfma_f32_16x16x32_bf16 v[52:55], v[218:221], v[162:165], v[52:55]
	v_mfma_f32_16x16x32_bf16 v[40:43], v[210:213], v[170:173], v[40:43]
	v_mfma_f32_16x16x32_bf16 v[36:39], v[218:221], v[170:173], v[36:39]
	v_mfma_f32_16x16x32_bf16 v[24:27], v[210:213], v[194:197], v[24:27]
	v_mfma_f32_16x16x32_bf16 v[20:23], v[218:221], v[194:197], v[20:23]
	v_mfma_f32_16x16x32_bf16 v[8:11], v[210:213], v[202:205], v[8:11]
	v_mfma_f32_16x16x32_bf16 v[4:7], v[218:221], v[202:205], v[4:7]
	s_setprio 0
	s_add_i32 s64, 0, 0x18000
	v_add_u32_e32 v0, s64, v137
	s_waitcnt vmcnt(10)
	s_barrier
	ds_read_b128 v[140:143], v0
	ds_read_b128 v[146:149], v0 offset:1024
	ds_read_b128 v[150:153], v0 offset:2048
	ds_read_b128 v[154:157], v0 offset:3072
	s_add_u32 s66, s69, s0
	s_addc_u32 s39, s39, s1
	s_add_u32 s66, s66, s15
	s_addc_u32 s67, s39, s14
	v_mov_b32_e32 v0, v132
	s_mov_b32 m0, s52
	ds_read_b128 v[158:161], v139 offset:32768
	ds_read_b128 v[162:165], v139 offset:33792
	ds_read_b128 v[166:169], v139 offset:34816
	ds_read_b128 v[170:173], v139 offset:35840
	ds_read_b128 v[190:193], v139 offset:36864
	ds_read_b128 v[194:197], v139 offset:37888
	ds_read_b128 v[198:201], v139 offset:38912
	ds_read_b128 v[202:205], v139 offset:39936
	s_nop 0
	global_load_lds_dwordx4 v0, s[66:67]
	v_mov_b32_e32 v0, v134
	s_mov_b32 m0, s53
	s_nop 0
	global_load_lds_dwordx4 v0, s[66:67]
	s_waitcnt lgkmcnt(8)
	s_barrier
	s_waitcnt lgkmcnt(0)
	s_setprio 1
	s_waitcnt lgkmcnt(0)
	v_mfma_f32_16x16x32_bf16 v[128:131], v[140:143], v[158:161], v[128:131]
	v_mfma_f32_16x16x32_bf16 v[124:127], v[150:153], v[158:161], v[124:127]
	v_mfma_f32_16x16x32_bf16 v[112:115], v[140:143], v[166:169], v[112:115]
	v_mfma_f32_16x16x32_bf16 v[108:111], v[150:153], v[166:169], v[108:111]
	v_mfma_f32_16x16x32_bf16 v[96:99], v[140:143], v[190:193], v[96:99]
	v_mfma_f32_16x16x32_bf16 v[92:95], v[150:153], v[190:193], v[92:95]
	v_mfma_f32_16x16x32_bf16 v[80:83], v[140:143], v[198:201], v[80:83]
	v_mfma_f32_16x16x32_bf16 v[76:79], v[150:153], v[198:201], v[76:79]
	v_mfma_f32_16x16x32_bf16 v[128:131], v[146:149], v[162:165], v[128:131]
	v_mfma_f32_16x16x32_bf16 v[124:127], v[154:157], v[162:165], v[124:127]
	v_mfma_f32_16x16x32_bf16 v[112:115], v[146:149], v[170:173], v[112:115]
	v_mfma_f32_16x16x32_bf16 v[108:111], v[154:157], v[170:173], v[108:111]
	v_mfma_f32_16x16x32_bf16 v[96:99], v[146:149], v[194:197], v[96:99]
	v_mfma_f32_16x16x32_bf16 v[92:95], v[154:157], v[194:197], v[92:95]
	v_mfma_f32_16x16x32_bf16 v[80:83], v[146:149], v[202:205], v[80:83]
	v_mfma_f32_16x16x32_bf16 v[76:79], v[154:157], v[202:205], v[76:79]
	s_setprio 0
	s_waitcnt vmcnt(10)
	s_barrier
	s_add_i32 s14, 0, 0x1c000
	s_add_u32 s24, s24, 0x80
	v_add_u32_e32 v0, s14, v137
	s_addc_u32 s25, s25, 0
	ds_read_b128 v[206:209], v0
	ds_read_b128 v[210:213], v0 offset:1024
	ds_read_b128 v[214:217], v0 offset:2048
	ds_read_b128 v[218:221], v0 offset:3072
	s_mov_b64 s[66:67], s[24:25]
	v_mov_b32_e32 v0, v133
	s_add_i32 s15, s64, s17
	s_mov_b32 m0, s15
	s_nop 0
	global_load_lds_dwordx4 v0, s[66:67]
	v_mov_b32_e32 v0, v135
	s_add_i32 m0, s15, 0x2000
	s_nop 0
	global_load_lds_dwordx4 v0, s[66:67]
	s_barrier
; #define PG8_STAGEA(bufoff, hh, kb, nx) do { if constexpr (Sched::GATHER) { unsigned _o[2]; _o[0] = (nx) ? vN[hh][0] : vC[hh][0]; _o[1] = (nx) ? vN[hh][1] : vC[hh][1]; PG8_STAGE(bufoff, cA + (kb), _o); } \
;         else { PG8_STAGE(bufoff, ((nx) ? nA : cA) + (hh) * hstep + (kb), voffA); } } while (0)
; template <class Epi, class Sched>
; __device__ __forceinline__ void gemm_phase(LAS unsigned char* lds, const int K_, const Sched& S, const Epi& E, const int wave_) {
;     ...
;         if (Epi::NSTORE > 0 && hoisted) { PG8_BODY(true); t = 2; }
;         for (; t < nt; t += 2) { PG8_BODY(false); }
;         hoisted = false;
;         if constexpr (Epi::NSTORE > 0) { if (has_next) { PG8_STAGEA(PG8_SA(1, 1), 1, kstep, true); hoisted = true; } }
	s_waitcnt lgkmcnt(0)
	s_setprio 1
	s_waitcnt lgkmcnt(0)
	v_mfma_f32_16x16x32_bf16 v[120:123], v[206:209], v[158:161], v[120:123]
	v_mfma_f32_16x16x32_bf16 v[116:119], v[214:217], v[158:161], v[116:119]
	v_mfma_f32_16x16x32_bf16 v[104:107], v[206:209], v[166:169], v[104:107]
	v_mfma_f32_16x16x32_bf16 v[100:103], v[214:217], v[166:169], v[100:103]
	v_mfma_f32_16x16x32_bf16 v[88:91], v[206:209], v[190:193], v[88:91]
	v_mfma_f32_16x16x32_bf16 v[84:87], v[214:217], v[190:193], v[84:87]
	v_mfma_f32_16x16x32_bf16 v[72:75], v[206:209], v[198:201], v[72:75]
	v_mfma_f32_16x16x32_bf16 v[68:71], v[214:217], v[198:201], v[68:71]
	v_mfma_f32_16x16x32_bf16 v[120:123], v[210:213], v[162:165], v[120:123]
	v_mfma_f32_16x16x32_bf16 v[116:119], v[218:221], v[162:165], v[116:119]
	v_mfma_f32_16x16x32_bf16 v[104:107], v[210:213], v[170:173], v[104:107]
	v_mfma_f32_16x16x32_bf16 v[100:103], v[218:221], v[170:173], v[100:103]
	v_mfma_f32_16x16x32_bf16 v[88:91], v[210:213], v[194:197], v[88:91]
	v_mfma_f32_16x16x32_bf16 v[84:87], v[218:221], v[194:197], v[84:87]
	v_mfma_f32_16x16x32_bf16 v[72:75], v[210:213], v[202:205], v[72:75]
	v_mfma_f32_16x16x32_bf16 v[68:71], v[218:221], v[202:205], v[68:71]
	s_setprio 0
	s_add_u32 s50, s50, 0x80
	s_addc_u32 s51, s51, 0
	v_mov_b32_e32 v0, v132
	s_mov_b32 m0, s55
	s_waitcnt vmcnt(10)
	s_barrier
	ds_read_b128 v[158:161], v139 offset:49152
	ds_read_b128 v[162:165], v139 offset:50176
	ds_read_b128 v[166:169], v139 offset:51200
	ds_read_b128 v[170:173], v139 offset:52224
	ds_read_b128 v[190:193], v139 offset:53248
	ds_read_b128 v[194:197], v139 offset:54272
	ds_read_b128 v[198:201], v139 offset:55296
	ds_read_b128 v[202:205], v139 offset:56320
	s_nop 0
	global_load_lds_dwordx4 v0, s[50:51]
	v_mov_b32_e32 v0, v134
	s_mov_b32 m0, s56
	s_nop 0
	global_load_lds_dwordx4 v0, s[50:51]
	s_barrier
	s_waitcnt lgkmcnt(0)
	s_setprio 1
	s_waitcnt lgkmcnt(0)
	v_mfma_f32_16x16x32_bf16 v[64:67], v[140:143], v[158:161], v[64:67]
	v_mfma_f32_16x16x32_bf16 v[60:63], v[150:153], v[158:161], v[60:63]
	v_mfma_f32_16x16x32_bf16 v[48:51], v[140:143], v[166:169], v[48:51]
	v_mfma_f32_16x16x32_bf16 v[44:47], v[150:153], v[166:169], v[44:47]
	v_mfma_f32_16x16x32_bf16 v[32:35], v[140:143], v[190:193], v[32:35]
	v_mfma_f32_16x16x32_bf16 v[28:31], v[150:153], v[190:193], v[28:31]
	v_mfma_f32_16x16x32_bf16 v[16:19], v[140:143], v[198:201], v[16:19]
	v_mfma_f32_16x16x32_bf16 v[12:15], v[150:153], v[198:201], v[12:15]
	v_mfma_f32_16x16x32_bf16 v[64:67], v[146:149], v[162:165], v[64:67]
	v_mfma_f32_16x16x32_bf16 v[60:63], v[154:157], v[162:165], v[60:63]
	v_mfma_f32_16x16x32_bf16 v[48:51], v[146:149], v[170:173], v[48:51]
	v_mfma_f32_16x16x32_bf16 v[44:47], v[154:157], v[170:173], v[44:47]
	v_mfma_f32_16x16x32_bf16 v[32:35], v[146:149], v[194:197], v[32:35]
	v_mfma_f32_16x16x32_bf16 v[28:31], v[154:157], v[194:197], v[28:31]
	v_mfma_f32_16x16x32_bf16 v[16:19], v[146:149], v[202:205], v[16:19]
	v_mfma_f32_16x16x32_bf16 v[12:15], v[154:157], v[202:205], v[12:15]
	s_setprio 0
	s_barrier
	s_add_u32 s24, s24, s4
	s_addc_u32 s25, s25, s5
	v_mov_b32_e32 v0, v133
	s_add_i32 s14, s14, s17
	s_mov_b32 m0, s14
	s_nop 0
	global_load_lds_dwordx4 v0, s[24:25]
	v_mov_b32_e32 v0, v135
	s_add_i32 m0, s14, 0x2000
	s_nop 0
	global_load_lds_dwordx4 v0, s[24:25]
	s_barrier
	s_setprio 1
	v_mfma_f32_16x16x32_bf16 v[56:59], v[206:209], v[158:161], v[56:59]
	v_mfma_f32_16x16x32_bf16 v[52:55], v[214:217], v[158:161], v[52:55]
	v_mfma_f32_16x16x32_bf16 v[40:43], v[206:209], v[166:169], v[40:43]
	v_mfma_f32_16x16x32_bf16 v[36:39], v[214:217], v[166:169], v[36:39]
	v_mfma_f32_16x16x32_bf16 v[24:27], v[206:209], v[190:193], v[24:27]
	v_mfma_f32_16x16x32_bf16 v[20:23], v[214:217], v[190:193], v[20:23]
	v_mfma_f32_16x16x32_bf16 v[8:11], v[206:209], v[198:201], v[8:11]
	v_mfma_f32_16x16x32_bf16 v[4:7], v[214:217], v[198:201], v[4:7]
	v_mfma_f32_16x16x32_bf16 v[56:59], v[210:213], v[162:165], v[56:59]
	v_mfma_f32_16x16x32_bf16 v[52:55], v[218:221], v[162:165], v[52:55]
	v_mfma_f32_16x16x32_bf16 v[40:43], v[210:213], v[170:173], v[40:43]
	v_mfma_f32_16x16x32_bf16 v[36:39], v[218:221], v[170:173], v[36:39]
	v_mfma_f32_16x16x32_bf16 v[24:27], v[210:213], v[194:197], v[24:27]
	v_mfma_f32_16x16x32_bf16 v[20:23], v[218:221], v[194:197], v[20:23]
	v_mfma_f32_16x16x32_bf16 v[8:11], v[210:213], v[202:205], v[8:11]
	v_mfma_f32_16x16x32_bf16 v[4:7], v[218:221], v[202:205], v[4:7]
	s_setprio 0
	s_add_u32 s29, s29, 0x100
	s_addc_u32 s30, s30, 0
	s_cmp_lt_i32 s31, s54
	s_mov_b32 s24, s31
	s_waitcnt vmcnt(10)
	s_barrier
	s_cbranch_scc1 .LBB0_1628
	s_waitcnt vmcnt(6)
	s_mov_b32 s39, 0x8000
	s_and_b64 vcc, exec, s[40:41]
	s_cbranch_vccz .LBB0_1633
	s_branch .LBB0_1634
